# prep: cq/u output pointers loaded at path entry instead of after the reduction barrier
# speedup vs baseline: 1.0084x; 1.0056x over previous
.LBB0_25:
	s_and_b64 vcc, exec, s[8:9]
	s_cbranch_vccz .LBB0_40
	s_load_dwordx4 s[20:23], s[0:1], 0x48
	s_lshl_b32 s8, s2, 6
	s_and_b32 s8, s8, 0xc0
	v_and_or_b32 v1, v0, 63, s8
	s_and_b32 s8, s2, 0x1fc
	s_cmpk_eq_i32 s8, 0x180
	s_cselect_b64 s[8:9], -1, 0
	v_and_b32_e32 v4, 0xc0, v0
	s_and_b64 s[10:11], s[8:9], exec
	v_lshlrev_b32_e32 v1, 2, v1
	s_waitcnt lgkmcnt(0)
	s_cselect_b32 s11, s7, s5
	s_cselect_b32 s10, s6, s4
	v_lshl_or_b32 v12, v4, 10, v1
	s_cselect_b32 s13, s13, s15
	s_cselect_b32 s12, s12, s14
	v_lshlrev_b32_e32 v47, 2, v4
	global_load_dword v32, v12, s[10:11]
	global_load_dword v44, v12, s[10:11] offset:1024
	global_load_dword v45, v12, s[10:11] offset:2048
	global_load_dwordx4 v[4:7], v47, s[12:13] offset:16
	global_load_dwordx4 v[8:11], v47, s[12:13]
	v_mov_b32_e32 v13, 0
	v_lshl_add_u64 v[2:3], s[10:11], 0, v[12:13]
	s_movk_i32 s16, 0x1000
	v_add_co_u32_e32 v14, vcc, s16, v2
	s_movk_i32 s14, 0x2000
	s_nop 0
	v_addc_co_u32_e32 v15, vcc, 0, v3, vcc
	v_add_co_u32_e32 v20, vcc, s14, v2
	s_movk_i32 s14, 0x3000
	s_nop 0
	v_addc_co_u32_e32 v21, vcc, 0, v3, vcc
	global_load_dword v46, v[14:15], off offset:1024
	global_load_dword v48, v[14:15], off offset:2048
	global_load_dword v49, v[14:15], off offset:3072
	global_load_dword v50, v12, s[10:11] offset:3072
	global_load_dword v51, v[20:21], off offset:-4096
	global_load_dword v52, v[20:21], off
	global_load_dword v53, v[20:21], off offset:1024
	global_load_dword v54, v[20:21], off offset:2048
	v_add_co_u32_e32 v22, vcc, s14, v2
	s_movk_i32 s14, 0x4000
	s_nop 0
	v_addc_co_u32_e32 v23, vcc, 0, v3, vcc
	v_add_co_u32_e32 v24, vcc, s14, v2
	s_movk_i32 s14, 0x5000
	s_nop 0
	v_addc_co_u32_e32 v25, vcc, 0, v3, vcc
	v_add_co_u32_e32 v36, vcc, s14, v2
	s_movk_i32 s14, 0x6000
	s_nop 0
	v_addc_co_u32_e32 v37, vcc, 0, v3, vcc
	v_add_co_u32_e32 v28, vcc, s14, v2
	s_movk_i32 s14, 0x7000
	s_nop 0
	v_addc_co_u32_e32 v29, vcc, 0, v3, vcc
	global_load_dword v55, v[22:23], off offset:1024
	global_load_dword v56, v[22:23], off offset:2048
	global_load_dword v57, v[22:23], off offset:3072
	global_load_dword v60, v[36:37], off offset:1024
	global_load_dword v61, v[36:37], off offset:2048
	global_load_dwordx4 v[12:15], v47, s[12:13] offset:48
	global_load_dwordx4 v[16:19], v47, s[12:13] offset:32
	global_load_dword v58, v[20:21], off offset:3072
	global_load_dword v59, v[24:25], off offset:-4096
	global_load_dword v62, v[24:25], off
	global_load_dword v63, v[24:25], off offset:1024
	global_load_dword v64, v[24:25], off offset:2048
	global_load_dword v65, v[24:25], off offset:3072
	global_load_dword v66, v[28:29], off offset:-4096
	global_load_dword v67, v[28:29], off
	v_add_co_u32_e32 v38, vcc, s14, v2
	s_mov_b32 s14, 0x8000
	s_nop 0
	v_addc_co_u32_e32 v39, vcc, 0, v3, vcc
	v_add_co_u32_e32 v30, vcc, s14, v2
	s_mov_b32 s14, 0x9000
	s_nop 0
	v_addc_co_u32_e32 v31, vcc, 0, v3, vcc
	global_load_dwordx4 v[20:23], v47, s[12:13] offset:80
	global_load_dwordx4 v[24:27], v47, s[12:13] offset:64
	global_load_dword v68, v[28:29], off offset:1024
	global_load_dword v69, v[28:29], off offset:2048
	global_load_dword v70, v[28:29], off offset:3072
	global_load_dword v71, v[30:31], off offset:-4096
	global_load_dword v72, v[30:31], off
	global_load_dword v73, v[30:31], off offset:1024
	global_load_dword v74, v[30:31], off offset:2048
	global_load_dword v75, v[30:31], off offset:3072
	v_add_co_u32_e32 v40, vcc, s14, v2
	s_mov_b32 s14, 0xa000
	s_nop 0
	v_addc_co_u32_e32 v41, vcc, 0, v3, vcc
	v_add_co_u32_e32 v42, vcc, s14, v2
	s_mov_b32 s14, 0xb000
	s_nop 0
	v_addc_co_u32_e32 v43, vcc, 0, v3, vcc
	s_waitcnt vmcnt(33)
	v_fma_f32 v76, v32, v8, 0
	global_load_dwordx4 v[28:31], v47, s[12:13] offset:112
	global_load_dwordx4 v[32:35], v47, s[12:13] offset:96
	v_fmac_f32_e32 v76, v44, v9
	v_add_co_u32_e32 v8, vcc, s14, v2
	v_fmac_f32_e32 v76, v45, v10
	s_nop 0
	v_addc_co_u32_e32 v9, vcc, 0, v3, vcc
	s_mov_b32 s14, 0xc000
	v_add_co_u32_e32 v44, vcc, s14, v2
	s_waitcnt vmcnt(31)
	v_fmac_f32_e32 v76, v50, v11
	v_addc_co_u32_e32 v45, vcc, 0, v3, vcc
	s_waitcnt vmcnt(30)
	v_fmac_f32_e32 v76, v51, v4
	s_mov_b32 s14, 0xd000
	global_load_dword v77, v[36:37], off offset:3072
	global_load_dword v78, v[38:39], off offset:1024
	global_load_dword v79, v[38:39], off offset:2048
	global_load_dword v80, v[38:39], off offset:3072
	global_load_dword v81, v[40:41], off offset:1024
	global_load_dword v82, v[40:41], off offset:2048
	global_load_dword v83, v[40:41], off offset:3072
	global_load_dword v84, v[8:9], off offset:1024
	v_fmac_f32_e32 v76, v46, v5
	v_add_co_u32_e32 v4, vcc, s14, v2
	v_fmac_f32_e32 v76, v48, v6
	s_nop 0
	v_addc_co_u32_e32 v5, vcc, 0, v3, vcc
	v_fmac_f32_e32 v76, v49, v7
	global_load_dword v85, v[42:43], off offset:-4096
	global_load_dword v86, v[42:43], off
	global_load_dword v87, v[42:43], off offset:1024
	global_load_dword v88, v[42:43], off offset:2048
	global_load_dword v89, v[42:43], off offset:3072
	global_load_dword v90, v[44:45], off offset:-4096
	global_load_dword v91, v[44:45], off
	global_load_dword v92, v[44:45], off offset:1024
	global_load_dword v93, v[8:9], off offset:2048
	global_load_dword v94, v[8:9], off offset:3072
	global_load_dword v49, v[4:5], off offset:1024
	global_load_dword v50, v[4:5], off offset:2048
	global_load_dword v51, v[4:5], off offset:3072
	s_nop 0
	global_load_dwordx4 v[4:7], v47, s[12:13] offset:144
	global_load_dwordx4 v[8:11], v47, s[12:13] offset:128
	s_waitcnt vmcnt(43)
	v_fmac_f32_e32 v76, v52, v16
	v_fmac_f32_e32 v76, v53, v17
	v_fmac_f32_e32 v76, v54, v18
	s_waitcnt vmcnt(42)
	v_fmac_f32_e32 v76, v58, v19
	s_waitcnt vmcnt(41)
	v_fmac_f32_e32 v76, v59, v12
	s_mov_b32 s14, 0xe000
	v_fmac_f32_e32 v76, v55, v13
	v_add_co_u32_e32 v36, vcc, s14, v2
	v_fmac_f32_e32 v76, v56, v14
	s_nop 0
	v_addc_co_u32_e32 v37, vcc, 0, v3, vcc
	v_fmac_f32_e32 v76, v57, v15
	global_load_dwordx4 v[12:15], v47, s[12:13] offset:176
	global_load_dwordx4 v[16:19], v47, s[12:13] offset:160
	global_load_dword v95, v[44:45], off offset:2048
	global_load_dword v96, v[44:45], off offset:3072
	global_load_dword v48, v[36:37], off offset:-4096
	global_load_dword v52, v[36:37], off
	global_load_dword v53, v[36:37], off offset:1024
	global_load_dword v54, v[36:37], off offset:2048
	global_load_dword v55, v[36:37], off offset:3072
	s_waitcnt vmcnt(42)
	v_fmac_f32_e32 v76, v62, v24
	global_load_dwordx4 v[36:39], v47, s[12:13] offset:192
	v_fmac_f32_e32 v76, v63, v25
	v_fmac_f32_e32 v76, v64, v26
	v_fmac_f32_e32 v76, v65, v27
	global_load_dwordx4 v[24:27], v47, s[12:13] offset:208
	s_mov_b32 s14, 0xf000
	v_add_co_u32_e32 v2, vcc, s14, v2
	s_mov_b32 s14, 0xfc00
	s_nop 0
	v_addc_co_u32_e32 v3, vcc, 0, v3, vcc
	global_load_dwordx3 v[44:46], v47, s[12:13] offset:240
	global_load_dwordx4 v[40:43], v47, s[12:13] offset:224
	global_load_dword v56, v[2:3], off
	global_load_dword v57, v[2:3], off offset:1024
	global_load_dword v58, v[2:3], off offset:2048
	v_lshlrev_b32_e32 v2, 10, v0
	v_or3_b32 v2, v2, v1, s14
	global_load_dword v59, v2, s[10:11]
	v_lshlrev_b32_e32 v2, 2, v0
	v_or_b32_e32 v3, 0xfc, v2
	global_load_dword v47, v3, s[12:13]
	v_fmac_f32_e32 v76, v66, v20
	v_fmac_f32_e32 v76, v60, v21
	v_fmac_f32_e32 v76, v61, v22
	v_cmp_gt_u32_e32 vcc, 64, v0
	s_waitcnt vmcnt(40)
	v_fmac_f32_e32 v76, v77, v23
	v_fmac_f32_e32 v76, v67, v32
	v_fmac_f32_e32 v76, v68, v33
	v_fmac_f32_e32 v76, v69, v34
	v_fmac_f32_e32 v76, v70, v35
	v_fmac_f32_e32 v76, v71, v28
	s_waitcnt vmcnt(39)
	v_fmac_f32_e32 v76, v78, v29
	s_waitcnt vmcnt(38)
	v_fmac_f32_e32 v76, v79, v30
	s_waitcnt vmcnt(37)
	v_fmac_f32_e32 v76, v80, v31
	s_waitcnt vmcnt(18)
	v_fmac_f32_e32 v76, v72, v8
	v_fmac_f32_e32 v76, v73, v9
	v_fmac_f32_e32 v76, v74, v10
	v_fmac_f32_e32 v76, v75, v11
	v_fmac_f32_e32 v76, v85, v4
	v_fmac_f32_e32 v76, v81, v5
	v_fmac_f32_e32 v76, v82, v6
	v_fmac_f32_e32 v76, v83, v7
	s_waitcnt vmcnt(16)
	v_fmac_f32_e32 v76, v86, v16
	v_fmac_f32_e32 v76, v87, v17
	v_fmac_f32_e32 v76, v88, v18
	v_fmac_f32_e32 v76, v89, v19
	v_fmac_f32_e32 v76, v90, v12
	v_fmac_f32_e32 v76, v84, v13
	v_fmac_f32_e32 v76, v93, v14
	v_fmac_f32_e32 v76, v94, v15
	s_waitcnt vmcnt(8)
	v_fmac_f32_e32 v76, v91, v36
	v_fmac_f32_e32 v76, v92, v37
	v_fmac_f32_e32 v76, v95, v38
	v_fmac_f32_e32 v76, v96, v39
	s_waitcnt vmcnt(7)
	v_pk_mul_f32 v[4:5], v[48:49], v[24:25]
	s_nop 0
	v_add_f32_e32 v3, v76, v4
	v_add_f32_e32 v3, v3, v5
	v_pk_mul_f32 v[4:5], v[50:51], v[26:27]
	s_nop 0
	v_add_f32_e32 v3, v3, v4
	v_add_f32_e32 v3, v3, v5
	s_waitcnt vmcnt(5)
	v_pk_mul_f32 v[4:5], v[52:53], v[40:41]
	s_nop 0
	v_add_f32_e32 v3, v3, v4
	v_add_f32_e32 v3, v3, v5
	v_pk_mul_f32 v[4:5], v[54:55], v[42:43]
	s_nop 0
	v_add_f32_e32 v3, v3, v4
	v_add_f32_e32 v3, v3, v5
	s_waitcnt vmcnt(3)
	v_pk_mul_f32 v[4:5], v[56:57], v[44:45]
	s_nop 0
	v_add_f32_e32 v3, v3, v4
	v_add_f32_e32 v3, v3, v5
	s_waitcnt vmcnt(0)
	v_pk_mul_f32 v[4:5], v[58:59], v[46:47]
	s_nop 0
	v_add_f32_e32 v3, v3, v4
	v_add_f32_e32 v3, v3, v5
	ds_write_b32 v2, v3
	s_waitcnt lgkmcnt(0)
	s_barrier
	s_and_saveexec_b64 s[10:11], vcc
	s_cbranch_execz .LBB0_28
	ds_read2st64_b32 v[4:5], v2 offset1:1
	ds_read2st64_b32 v[2:3], v2 offset0:2 offset1:3
	s_and_b64 s[8:9], s[8:9], exec
	s_waitcnt lgkmcnt(0)
	v_add_f32_e32 v4, v4, v5
	v_add_f32_e32 v2, v4, v2
	s_cselect_b32 s9, s21, s23
	v_add_f32_e32 v2, v2, v3
	s_cselect_b32 s8, s20, s22
	global_store_dword v1, v2, s[8:9]

	.amdhsa_kernel _Z7na_prepPKfS0_S0_S0_S0_S0_PDF16_PhS1_PfS3_S3_
		.amdhsa_group_segment_fixed_size 50176
		.amdhsa_private_segment_fixed_size 0
		.amdhsa_kernarg_size 96
		.amdhsa_user_sgpr_count 2
		.amdhsa_user_sgpr_dispatch_ptr 0
		.amdhsa_user_sgpr_queue_ptr 0
		.amdhsa_user_sgpr_kernarg_segment_ptr 1
		.amdhsa_user_sgpr_dispatch_id 0
		.amdhsa_user_sgpr_kernarg_preload_length 0
		.amdhsa_user_sgpr_kernarg_preload_offset 0
		.amdhsa_user_sgpr_private_segment_size 0
		.amdhsa_uses_dynamic_stack 0
		.amdhsa_enable_private_segment 0
		.amdhsa_system_sgpr_workgroup_id_x 1
		.amdhsa_system_sgpr_workgroup_id_y 0
		.amdhsa_system_sgpr_workgroup_id_z 0
		.amdhsa_system_sgpr_workgroup_info 0
		.amdhsa_system_vgpr_workitem_id 0
		.amdhsa_next_free_vgpr 116
		.amdhsa_next_free_sgpr 24
		.amdhsa_accum_offset 100
		.amdhsa_reserve_vcc 1
		.amdhsa_float_round_mode_32 0
		.amdhsa_float_round_mode_16_64 0
		.amdhsa_float_denorm_mode_32 3
		.amdhsa_float_denorm_mode_16_64 3
		.amdhsa_dx10_clamp 1
		.amdhsa_ieee_mode 1
		.amdhsa_fp16_overflow 0
		.amdhsa_tg_split 0
		.amdhsa_exception_fp_ieee_invalid_op 0
		.amdhsa_exception_fp_denorm_src 0
		.amdhsa_exception_fp_ieee_div_zero 0
		.amdhsa_exception_fp_ieee_overflow 0
		.amdhsa_exception_fp_ieee_underflow 0
		.amdhsa_exception_fp_ieee_inexact 0
		.amdhsa_exception_int_div_zero 0
	.end_amdhsa_kernel

amdhsa.kernels:
  - .agpr_count:     16
    .args:
      - .actual_access:  read_only
        .address_space:  global
        .offset:         0
        .size:           8
        .value_kind:     global_buffer
      - .actual_access:  read_only
        .address_space:  global
        .offset:         8
        .size:           8
        .value_kind:     global_buffer
      - .actual_access:  read_only
        .address_space:  global
        .offset:         16
        .size:           8
        .value_kind:     global_buffer
      - .actual_access:  read_only
        .address_space:  global
        .offset:         24
        .size:           8
        .value_kind:     global_buffer
      - .actual_access:  read_only
        .address_space:  global
        .offset:         32
        .size:           8
        .value_kind:     global_buffer
      - .actual_access:  read_only
        .address_space:  global
        .offset:         40
        .size:           8
        .value_kind:     global_buffer
      - .actual_access:  write_only
        .address_space:  global
        .offset:         48
        .size:           8
        .value_kind:     global_buffer
      - .actual_access:  write_only
        .address_space:  global
        .offset:         56
        .size:           8
        .value_kind:     global_buffer
      - .actual_access:  write_only
        .address_space:  global
        .offset:         64
        .size:           8
        .value_kind:     global_buffer
      - .actual_access:  write_only
        .address_space:  global
        .offset:         72
        .size:           8
        .value_kind:     global_buffer
      - .actual_access:  write_only
        .address_space:  global
        .offset:         80
        .size:           8
        .value_kind:     global_buffer
      - .actual_access:  write_only
        .address_space:  global
        .offset:         88
        .size:           8
        .value_kind:     global_buffer
    .group_segment_fixed_size: 50176
    .kernarg_segment_align: 8
    .kernarg_segment_size: 96
    .language:       OpenCL C
    .language_version:
      - 2
      - 0
    .max_flat_workgroup_size: 256
    .name:           _Z7na_prepPKfS0_S0_S0_S0_S0_PDF16_PhS1_PfS3_S3_
    .private_segment_fixed_size: 0
    .sgpr_count:     30
    .sgpr_spill_count: 0
    .symbol:         _Z7na_prepPKfS0_S0_S0_S0_S0_PDF16_PhS1_PfS3_S3_.kd
    .uniform_work_group_size: 1
    .uses_dynamic_stack: false
    .vgpr_count:     116
    .vgpr_spill_count: 0
    .wavefront_size: 64
  - .agpr_count:     0
    .args:
      - .address_space:  global
        .offset:         0
        .size:           8
        .value_kind:     global_buffer
      - .actual_access:  read_only
        .address_space:  global
        .offset:         8
        .size:           8
        .value_kind:     global_buffer
      - .actual_access:  read_only
        .address_space:  global
        .offset:         16
        .size:           8
        .value_kind:     global_buffer
      - .actual_access:  read_only
        .address_space:  global
        .offset:         24
        .size:           8
        .value_kind:     global_buffer
      - .actual_access:  read_only
        .address_space:  global
        .offset:         32
        .size:           8
        .value_kind:     global_buffer
      - .actual_access:  read_only
        .address_space:  global
        .offset:         40
        .size:           8
        .value_kind:     global_buffer
      - .actual_access:  read_only
        .address_space:  global
        .offset:         48
        .size:           8
        .value_kind:     global_buffer
      - .actual_access:  write_only
        .address_space:  global
        .offset:         56
        .size:           8
        .value_kind:     global_buffer
    .group_segment_fixed_size: 162048
    .kernarg_segment_align: 8
    .kernarg_segment_size: 64
    .language:       OpenCL C
    .language_version:
      - 2
      - 0
    .max_flat_workgroup_size: 512
    .name:           _Z7na_mainPKDF16_PKhS0_PKfS4_S4_S4_Pf
    .private_segment_fixed_size: 0
    .sgpr_count:     42
    .sgpr_spill_count: 0
    .symbol:         _Z7na_mainPKDF16_PKhS0_PKfS4_S4_S4_Pf.kd
    .uniform_work_group_size: 1
    .uses_dynamic_stack: false
    .vgpr_count:     252
    .vgpr_spill_count: 0
    .wavefront_size: 64
